# waitcnt trim: always-satisfied vmcnt(2) after the conversion stores removed
# baseline (speedup 1.0000x reference)
; DEVI void cv_finish(char* img  , int lane, const CvRegs& R) {
;     ...
;     const int n = lane >> 1, half = lane & 1; u32x4 w0, w1;
; #pragma unroll
;     for (int j = 0; j < 4; ++j) { w0[j] = *(const unsigned*)(img + n * 68 + half * 32 + j * 4); w1[j] = *(const unsigned*)(img + n * 68 + half * 32 + 16 + j * 4); }
;     const int row = R.c.perm ? R.c.r0 + 128 * ((n >> 3) & 1) + 16 * ((n >> 2) & 1) + 4 * (n >> 4) + (n & 3) : R.c.r0 + 128 * ((n >> 2) & 1) + 4 * (n >> 3) + (n & 3);
;     bf16_t* d = R.c.dst + (size_t)row * R.c.K + R.c.k0 + half * 16;
;     __builtin_nontemporal_store(w0, (u32x4*)d); __builtin_nontemporal_store(w1, (u32x4*)(d + 8));
.Lmy_cvj_a:
	ds_read2_b32 v[66:67], v171 offset1:1
	ds_read2_b32 v[70:71], v171 offset0:4 offset1:5
	ds_read2_b32 v[72:73], v171 offset0:6 offset1:7
	ds_read2_b32 v[68:69], v171 offset0:2 offset1:3


; #define VM0() asm volatile("s_waitcnt vmcnt(0)" ::: "memory")
; DEVI void cv_finish(char* img  , int lane, const CvRegs& R) {
;     ...
;     bf16_t* d = R.c.dst + (size_t)row * R.c.K + R.c.k0 + half * 16;
;     __builtin_nontemporal_store(w0, (u32x4*)d); __builtin_nontemporal_store(w1, (u32x4*)(d + 8));
; DEVI void attn_unit8(const Params& p, char* smem, int unit, int l, int& cvs  , CvRun& crun) {
;     ...
;         if (cvr.live) asm volatile("s_waitcnt vmcnt(2)" ::: "memory"); else VM0();
	s_waitcnt lgkmcnt(0)
	global_store_dwordx4 v246, v[66:69], s[40:41] nt
	global_store_dwordx4 v246, v[70:73], s[40:41] offset:16 nt

; #define VM0() asm volatile("s_waitcnt vmcnt(0)" ::: "memory")
; DEVI void attn_unit8(const Params& p, char* smem, int unit, int l, int& cvs  , CvRun& crun) {
;     ...
;         if (cvr.live) asm volatile("s_waitcnt vmcnt(2)" ::: "memory"); else VM0();
;         __syncthreads();
;         if (T + 2 < NTILE) B_DMA(T + 2, s2);
	s_cbranch_execz .LBB0_701
	s_branch .LBB0_702
